# v30 + P7 LDS image in pieces of 8 rows x 128 B (full cache lines per LDS-DMA instruction), padded to v30's code placement modulo 64
# speedup vs baseline: 1.0074x; 1.0074x over previous
.LBB0_564:
	v_and_b32_e32 v234, 63, v0
	v_lshrrev_b32_e32 v233, 6, v0
	v_lshrrev_b32_e32 v226, 3, v234
	v_and_b32_e32 v232, 7, v234
	v_and_b32_e32 v227, 6, v226
	v_xor_b32_e32 v232, v232, v227
	v_lshlrev_b32_e32 v232, 4, v232
	v_lshl_add_u32 v228, v233, 3, v226
	v_add_u32_e32 v136, 0, v228
	v_lshl_add_u32 v136, v136, 12, v232
	v_add_u32_e32 v132, 64, v228
	v_lshl_add_u32 v132, v132, 12, v232
	v_mov_b32_e32 v138, v136
	v_mov_b32_e32 v140, v132
	v_and_b32_e32 v229, 31, v228
	v_bfe_u32 v230, v229, 2, 2
	v_lshlrev_b32_e32 v230, 3, v230
	v_bfe_u32 v231, v229, 4, 1
	v_lshl_add_u32 v230, v231, 2, v230
	v_and_b32_e32 v231, 3, v229
	v_add_u32_e32 v230, v230, v231
	v_add_u32_e32 v134, 0, v228
	v_and_b32_e32 v134, 0xffffffe0, v134
	v_add_u32_e32 v134, v134, v230
	v_lshl_add_u32 v134, v134, 12, v232
	v_add_u32_e32 v130, 64, v228
	v_and_b32_e32 v130, 0xffffffe0, v130
	v_add_u32_e32 v130, v130, v230
	v_lshl_add_u32 v130, v130, 12, v232
	v_and_b32_e32 v226, 15, v234
	v_lshrrev_b32_e32 v227, 4, v234
	v_and_b32_e32 v228, 6, v226
	v_xor_b32_e32 v227, v227, v228
	v_lshlrev_b32_e32 v227, 4, v227
	v_bfe_u32 v228, v226, 3, 1
	v_lshl_add_u32 v227, v228, 10, v227
	v_and_b32_e32 v228, 7, v226
	v_lshl_add_u32 v227, v228, 7, v227
	v_lshrrev_b32_e32 v228, 2, v233
	v_lshl_add_u32 v154, v228, 13, v227
	v_and_b32_e32 v228, 3, v233
	v_lshl_add_u32 v150, v228, 12, v227
	s_cmp_lt_i32 s90, 8
	s_cselect_b64 s[0:1], -1, 0
	s_cmp_gt_i32 s91, 7
	s_cselect_b64 s[2:3], -1, 0
	s_and_b64 s[0:1], s[0:1], s[2:3]
	s_andn2_b64 vcc, exec, s[0:1]
	s_cbranch_vccnz .LBB0_581
	s_cmpk_gt_i32 s87, 0xabf
	v_readfirstlane_b32 s5, v0
	s_cbranch_scc1 .LBB0_581
	v_lshrrev_b32_e32 v1, 5, v0
	s_waitcnt lgkmcnt(0)
	v_lshrrev_b32_e32 v3, 1, v0
	v_and_b32_e32 v1, 4, v1
	v_bfe_u32 v2, v0, 2, 2
	s_waitcnt vmcnt(6)
	v_and_b32_e32 v13, 24, v3
	s_add_u32 s28, s58, 0x59680000
	v_or3_b32 v1, v1, v2, v13
	v_lshlrev_b32_e32 v2, 4, v0
	s_addc_u32 s29, s59, 0
	v_or_b32_e32 v10, 0x2000, v2
	s_add_u32 s30, s58, 0x2200000
	v_lshrrev_b32_e32 v3, 7, v10
	s_movk_i32 s2, 0x60
	s_addc_u32 s31, s59, 0
	v_and_or_b32 v4, v3, s2, v1
	s_waitcnt vmcnt(5)
	v_bfe_u32 v14, v0, 2, 4
	s_movk_i32 s2, 0x70
	s_ashr_i32 s34, s87, 31
	v_and_or_b32 v3, v3, s2, v14
	s_lshr_b32 s2, s34, 29
	s_add_i32 s2, s87, s2
	s_lshr_b32 s8, s5, 6
	s_ashr_i32 s3, s2, 3
	s_and_b32 s2, s2, -8
	s_lshr_b32 s10, s5, 8
	s_lshl_b32 s33, s8, 10
	s_sub_i32 s2, s87, s2
	s_cmp_lt_i32 s2, 0
	s_movk_i32 s35, 0x159
	s_cselect_b32 s4, s35, 0x158
	s_mul_i32 s2, s2, s4
	s_add_i32 s2, s2, s3
	s_mul_hi_i32 s3, s2, 0x2fa0be83
	s_lshr_b32 s4, s3, 31
	s_ashr_i32 s3, s3, 5
	s_add_i32 s3, s3, s4
	s_lshl_b32 s6, s3, 2
	s_mulk_i32 s3, 0xac
	s_sub_i32 s2, s2, s3
	s_bfe_u32 s3, s2, 0x2001d
	s_add_i32 s3, s2, s3
	s_sext_i32_i16 s4, s3
	s_and_b32 s3, s3, 0xfffc
	s_sub_i32 s2, s2, s3
	s_sext_i32_i16 s2, s2
	v_and_b32_e32 v5, 32, v0
	s_lshr_b32 s4, s4, 2
	s_add_i32 s20, s6, s2
	v_bitop3_b32 v11, v2, v5, 48 bitop3:0x6c
	v_and_b32_e32 v12, 64, v0
	s_ashr_i32 s21, s20, 31
	s_bfe_i64 s[6:7], s[4:5], 0x100000
	v_or_b32_e32 v2, v11, v12
	s_lshl_b64 s[2:3], s[20:21], 20
	s_lshl_b64 s[6:7], s[6:7], 20
	v_lshrrev_b32_e32 v3, 3, v0
	s_add_u32 s24, s30, s6
	v_and_or_b32 v1, v3, 32, v1
	s_addc_u32 s25, s31, s7
	s_add_i32 s21, s33, 0
	s_add_i32 m0, s21, 0x10000
	global_load_lds_dwordx4 v134, s[24:25]
	s_add_i32 m0, s21, 0x12000
	s_add_u32 s6, s24, 0x80000
	global_load_lds_dwordx4 v130, s[24:25]
	s_addc_u32 s7, s25, 0
	s_add_i32 m0, s21, 0x14000
	v_and_or_b32 v1, v3, 48, v14
	global_load_lds_dwordx4 v134, s[6:7]
	s_add_i32 m0, s21, 0x16000
	s_add_u32 s22, s28, s2
	s_addc_u32 s23, s29, s3
	s_add_i32 s36, s21, 0x2000
	global_load_lds_dwordx4 v130, s[6:7]
	s_mov_b32 m0, s21
	s_add_u32 s2, s22, 0x80000
	global_load_lds_dwordx4 v136, s[22:23]
	s_mov_b32 m0, s36
	s_addc_u32 s3, s23, 0
	s_add_i32 s37, s21, 0x4000
	global_load_lds_dwordx4 v132, s[22:23]
	s_mov_b32 m0, s37
	s_add_i32 s42, s21, 0x6000
	global_load_lds_dwordx4 v136, s[2:3]
	s_mov_b32 m0, s42
	v_mov_b32_e32 v135, 0
	global_load_lds_dwordx4 v132, s[2:3]
	v_mov_b32_e32 v131, v135
	v_mov_b32_e32 v137, v135
	v_mov_b32_e32 v133, v135
	s_cmp_eq_u32 s10, 1
	s_mov_b32 s43, 0
	v_lshl_add_u64 v[8:9], s[24:25], 0, v[134:135]
	v_lshl_add_u64 v[6:7], s[24:25], 0, v[130:131]
	v_lshl_add_u64 v[2:3], s[22:23], 0, v[136:137]
	s_cselect_b64 s[2:3], -1, 0
	s_cmp_lg_u32 s10, 1
	v_lshl_add_u64 v[4:5], s[22:23], 0, v[132:133]
	s_cbranch_scc1 .LBB0_568
	s_barrier
.LBB0_568:
	s_add_u32 s6, s58, 0x65680000
	s_addc_u32 s7, s59, 0
	s_lshl_b32 s8, s8, 5
	s_and_b32 s14, s8, 0x60
	s_mov_b64 s[8:9], 0x80
	s_add_i32 m0, s21, 0x18000
	v_lshl_add_u64 v[8:9], v[8:9], 0, s[8:9]
	s_lshl_b32 s11, s10, 13
	s_lshl_b32 s15, s14, 7
	s_waitcnt vmcnt(2)
	s_barrier
	global_load_lds_dwordx4 v[8:9], off
	v_lshl_add_u64 v[6:7], v[6:7], 0, s[8:9]
	s_add_i32 m0, s21, 0x1a000
	s_add_i32 s44, s21, 0x8000
	s_add_i32 s45, s21, 0xa000
	global_load_lds_dwordx4 v[6:7], off
	v_lshl_add_u64 v[2:3], v[2:3], 0, s[8:9]
	s_mov_b32 m0, s44
	s_add_u32 s12, s24, 0x80080
	global_load_lds_dwordx4 v[2:3], off
	v_lshl_add_u64 v[2:3], v[4:5], 0, s[8:9]
	s_mov_b32 m0, s45
	s_addc_u32 s13, s25, 0
	global_load_lds_dwordx4 v[2:3], off
	s_add_i32 m0, s21, 0x1c000
	v_lshl_add_u64 v[2:3], s[12:13], 0, v[134:135]
	global_load_lds_dwordx4 v[2:3], off
	v_lshl_add_u64 v[2:3], s[12:13], 0, v[130:131]
	s_add_i32 m0, s21, 0x1e000
	s_sext_i32_i16 s64, s4
	global_load_lds_dwordx4 v[2:3], off
	v_and_b32_e32 v2, 15, v0
	v_lshlrev_b32_e32 v3, 1, v13
	v_lshlrev_b32_e32 v5, 6, v0
	s_movk_i32 s4, 0x3c0
	v_lshl_or_b32 v1, s10, 6, v2
	v_lshl_or_b32 v2, v2, 6, v3
	v_and_b32_e32 v4, 32, v244
	v_and_or_b32 v3, v5, s4, v3
	v_lshlrev_b32_e32 v3, 9, v0
	v_bitop3_b32 v2, v2, s11, v4 bitop3:0xde
	v_and_b32_e32 v3, 0x30000, v3
	v_lshlrev_b32_e32 v4, 12, v14
	v_or3_b32 v3, v11, v3, v4
	v_lshlrev_b32_e32 v3, 5, v10
	s_waitcnt vmcnt(6)
	s_cmpk_lt_u32 s5, 0x100
	v_and_b32_e32 v3, 0x70000, v3
	s_cselect_b64 s[10:11], -1, 0
	v_or3_b32 v3, v11, v3, v4
	s_add_i32 s61, 0, 0x10000
	s_add_i32 s62, 0, 0x14000
	s_ashr_i32 s60, s96, 31
	v_or_b32_e32 v151, s14, v13
	v_mov_b32_e32 v139, v135
	v_mov_b32_e32 v141, v135
	v_mov_b64_e32 v[142:143], 0xac0
	v_mov_b64_e32 v[144:145], 0xabf
	v_add_u32_e32 v152, s61, v150
	v_add_u32_e32 v153, s62, v150
	s_movk_i32 s63, 0x2b00
	s_barrier
	s_waitcnt vmcnt(0)
	v_xor_b32_e32 v227, 64, v152
	v_xor_b32_e32 v228, 64, v153
	v_xor_b32_e32 v229, 64, v154
	v_xor_b32_e32 v231, 64, v150
	s_branch .LBB0_571

.LBB0_574:
	ds_read_b128 v[146:149], v152
	ds_read_b128 v[156:159], v227
	ds_read_b128 v[160:163], v152 offset:2048
	ds_read_b128 v[164:167], v227 offset:2048
	ds_read_b128 v[168:171], v153
	ds_read_b128 v[172:175], v228
	ds_read_b128 v[176:179], v153 offset:2048
	ds_read_b128 v[180:183], v228 offset:2048
	s_add_u32 s24, s22, 0xfff80080
	s_addc_u32 s25, s23, -1
	s_cmp_eq_u32 s69, 28
	s_cselect_b32 s27, s15, s25
	s_cselect_b32 s26, s65, s24
	s_cselect_b32 s25, s13, s68
	s_cselect_b32 s24, s66, s67
	s_add_i32 m0, s21, 0xc000
	ds_read_b128 v[184:187], v154
	ds_read_b128 v[188:191], v229
	ds_read_b128 v[192:195], v154 offset:2048
	ds_read_b128 v[196:199], v229 offset:2048
	ds_read_b128 v[200:203], v154 offset:4096
	ds_read_b128 v[204:207], v229 offset:4096
	ds_read_b128 v[208:211], v154 offset:6144
	ds_read_b128 v[212:215], v229 offset:6144
	global_load_lds_dwordx4 v138, s[22:23]
	s_add_i32 m0, s21, 0xe000
	s_nop 0
	global_load_lds_dwordx4 v140, s[22:23]
	s_waitcnt vmcnt(8)
	s_waitcnt lgkmcnt(0)
	s_barrier
	s_setprio 1
	s_waitcnt lgkmcnt(0)
	v_mfma_f32_16x16x32_bf16 v[126:129], v[146:149], v[184:187], v[126:129]
	v_mfma_f32_16x16x32_bf16 v[122:125], v[160:163], v[184:187], v[122:125]
	v_mfma_f32_16x16x32_bf16 v[110:113], v[146:149], v[192:195], v[110:113]
	v_mfma_f32_16x16x32_bf16 v[106:109], v[160:163], v[192:195], v[106:109]
	v_mfma_f32_16x16x32_bf16 v[94:97], v[146:149], v[200:203], v[94:97]
	v_mfma_f32_16x16x32_bf16 v[90:93], v[160:163], v[200:203], v[90:93]
	v_mfma_f32_16x16x32_bf16 v[78:81], v[146:149], v[208:211], v[78:81]
	v_mfma_f32_16x16x32_bf16 v[74:77], v[160:163], v[208:211], v[74:77]
	v_mfma_f32_16x16x32_bf16 v[126:129], v[156:159], v[188:191], v[126:129]
	v_mfma_f32_16x16x32_bf16 v[122:125], v[164:167], v[188:191], v[122:125]
	v_mfma_f32_16x16x32_bf16 v[110:113], v[156:159], v[196:199], v[110:113]
	v_mfma_f32_16x16x32_bf16 v[106:109], v[164:167], v[196:199], v[106:109]
	v_mfma_f32_16x16x32_bf16 v[94:97], v[156:159], v[204:207], v[94:97]
	v_mfma_f32_16x16x32_bf16 v[90:93], v[164:167], v[204:207], v[90:93]
	v_mfma_f32_16x16x32_bf16 v[78:81], v[156:159], v[212:215], v[78:81]
	v_mfma_f32_16x16x32_bf16 v[74:77], v[164:167], v[212:215], v[74:77]
	s_setprio 0
	s_setprio 1
	v_mfma_f32_16x16x32_bf16 v[118:121], v[168:171], v[184:187], v[118:121]
	v_mfma_f32_16x16x32_bf16 v[114:117], v[176:179], v[184:187], v[114:117]
	v_mfma_f32_16x16x32_bf16 v[102:105], v[168:171], v[192:195], v[102:105]
	v_mfma_f32_16x16x32_bf16 v[98:101], v[176:179], v[192:195], v[98:101]
	v_mfma_f32_16x16x32_bf16 v[86:89], v[168:171], v[200:203], v[86:89]
	v_mfma_f32_16x16x32_bf16 v[82:85], v[176:179], v[200:203], v[82:85]
	v_mfma_f32_16x16x32_bf16 v[70:73], v[168:171], v[208:211], v[70:73]
	v_mfma_f32_16x16x32_bf16 v[66:69], v[176:179], v[208:211], v[66:69]
	v_mfma_f32_16x16x32_bf16 v[118:121], v[172:175], v[188:191], v[118:121]
	v_mfma_f32_16x16x32_bf16 v[114:117], v[180:183], v[188:191], v[114:117]
	v_mfma_f32_16x16x32_bf16 v[102:105], v[172:175], v[196:199], v[102:105]
	v_mfma_f32_16x16x32_bf16 v[98:101], v[180:183], v[196:199], v[98:101]
	v_mfma_f32_16x16x32_bf16 v[86:89], v[172:175], v[204:207], v[86:89]
	v_mfma_f32_16x16x32_bf16 v[82:85], v[180:183], v[204:207], v[82:85]
	v_mfma_f32_16x16x32_bf16 v[70:73], v[172:175], v[212:215], v[70:73]
	v_mfma_f32_16x16x32_bf16 v[66:69], v[180:183], v[212:215], v[66:69]
	s_setprio 0
	s_barrier
	s_add_i32 s70, s61, s33
	v_lshl_add_u64 v[216:217], s[24:25], 0, v[134:135]
	s_mov_b32 m0, s70
	ds_read_b128 v[184:187], v154 offset:16384
	ds_read_b128 v[188:191], v229 offset:16384
	ds_read_b128 v[192:195], v154 offset:18432
	ds_read_b128 v[196:199], v229 offset:18432
	ds_read_b128 v[200:203], v154 offset:20480
	ds_read_b128 v[204:207], v229 offset:20480
	ds_read_b128 v[208:211], v154 offset:22528
	ds_read_b128 v[212:215], v229 offset:22528
	global_load_lds_dwordx4 v134, s[24:25]
	s_add_i32 m0, s70, 0x2000
	s_add_u32 s70, s24, 0x80000
	v_lshl_add_u64 v[218:219], s[24:25], 0, v[130:131]
	s_addc_u32 s71, s25, 0
	s_add_i32 s72, s62, s33
	global_load_lds_dwordx4 v130, s[24:25]
	s_mov_b32 m0, s72
	v_lshl_add_u64 v[222:223], s[26:27], 0, v[132:133]
	global_load_lds_dwordx4 v134, s[70:71]
	s_add_i32 m0, s72, 0x2000
	s_nop 0
	global_load_lds_dwordx4 v130, s[70:71]
	v_lshl_add_u64 v[220:221], s[26:27], 0, v[136:137]
	s_mov_b32 m0, s21
	s_nop 0
	global_load_lds_dwordx4 v136, s[26:27]
	s_mov_b32 m0, s36
	s_nop 0
	global_load_lds_dwordx4 v132, s[26:27]
	s_waitcnt vmcnt(8)
	s_waitcnt lgkmcnt(0)
	s_barrier
	s_setprio 1
	s_waitcnt lgkmcnt(0)
	v_mfma_f32_16x16x32_bf16 v[62:65], v[146:149], v[184:187], v[62:65]
	v_mfma_f32_16x16x32_bf16 v[58:61], v[160:163], v[184:187], v[58:61]
	v_mfma_f32_16x16x32_bf16 v[46:49], v[146:149], v[192:195], v[46:49]
	v_mfma_f32_16x16x32_bf16 v[42:45], v[160:163], v[192:195], v[42:45]
	v_mfma_f32_16x16x32_bf16 v[30:33], v[146:149], v[200:203], v[30:33]
	v_mfma_f32_16x16x32_bf16 v[26:29], v[160:163], v[200:203], v[26:29]
	v_mfma_f32_16x16x32_bf16 v[14:17], v[146:149], v[208:211], v[14:17]
	v_mfma_f32_16x16x32_bf16 v[10:13], v[160:163], v[208:211], v[10:13]
	v_mfma_f32_16x16x32_bf16 v[62:65], v[156:159], v[188:191], v[62:65]
	v_mfma_f32_16x16x32_bf16 v[58:61], v[164:167], v[188:191], v[58:61]
	v_mfma_f32_16x16x32_bf16 v[46:49], v[156:159], v[196:199], v[46:49]
	v_mfma_f32_16x16x32_bf16 v[42:45], v[164:167], v[196:199], v[42:45]
	v_mfma_f32_16x16x32_bf16 v[30:33], v[156:159], v[204:207], v[30:33]
	v_mfma_f32_16x16x32_bf16 v[26:29], v[164:167], v[204:207], v[26:29]
	v_mfma_f32_16x16x32_bf16 v[14:17], v[156:159], v[212:215], v[14:17]
	v_mfma_f32_16x16x32_bf16 v[10:13], v[164:167], v[212:215], v[10:13]
	s_setprio 0
	s_setprio 1
	v_mfma_f32_16x16x32_bf16 v[54:57], v[168:171], v[184:187], v[54:57]
	v_mfma_f32_16x16x32_bf16 v[50:53], v[176:179], v[184:187], v[50:53]
	v_mfma_f32_16x16x32_bf16 v[38:41], v[168:171], v[192:195], v[38:41]
	v_mfma_f32_16x16x32_bf16 v[34:37], v[176:179], v[192:195], v[34:37]
	v_mfma_f32_16x16x32_bf16 v[22:25], v[168:171], v[200:203], v[22:25]
	v_mfma_f32_16x16x32_bf16 v[18:21], v[176:179], v[200:203], v[18:21]
	v_mfma_f32_16x16x32_bf16 v[6:9], v[168:171], v[208:211], v[6:9]
	v_mfma_f32_16x16x32_bf16 v[2:5], v[176:179], v[208:211], v[2:5]
	v_mfma_f32_16x16x32_bf16 v[54:57], v[172:175], v[188:191], v[54:57]
	v_mfma_f32_16x16x32_bf16 v[50:53], v[180:183], v[188:191], v[50:53]
	v_mfma_f32_16x16x32_bf16 v[38:41], v[172:175], v[196:199], v[38:41]
	v_mfma_f32_16x16x32_bf16 v[34:37], v[180:183], v[196:199], v[34:37]
	v_mfma_f32_16x16x32_bf16 v[22:25], v[172:175], v[204:207], v[22:25]
	v_mfma_f32_16x16x32_bf16 v[18:21], v[180:183], v[204:207], v[18:21]
	v_mfma_f32_16x16x32_bf16 v[6:9], v[172:175], v[212:215], v[6:9]
	v_mfma_f32_16x16x32_bf16 v[2:5], v[180:183], v[212:215], v[2:5]
	s_setprio 0
	s_barrier
	s_add_i32 s70, 0, 0x18000
	v_add_u32_e32 v155, s70, v150
	v_add_u32_e32 v230, s70, v231
	s_add_i32 s71, 0, 0x1c000
	ds_read_b128 v[146:149], v155
	ds_read_b128 v[156:159], v230
	ds_read_b128 v[160:163], v155 offset:2048
	ds_read_b128 v[164:167], v230 offset:2048
	v_add_u32_e32 v155, s71, v150
	v_add_u32_e32 v230, s71, v231
	ds_read_b128 v[168:171], v155
	ds_read_b128 v[172:175], v230
	ds_read_b128 v[176:179], v155 offset:2048
	ds_read_b128 v[180:183], v230 offset:2048
	s_add_u32 s26, s26, 0x80000
	s_addc_u32 s27, s27, 0
	s_mov_b32 m0, s37
	ds_read_b128 v[184:187], v154 offset:32768
	ds_read_b128 v[188:191], v229 offset:32768
	ds_read_b128 v[192:195], v154 offset:34816
	ds_read_b128 v[196:199], v229 offset:34816
	ds_read_b128 v[200:203], v154 offset:36864
	ds_read_b128 v[204:207], v229 offset:36864
	ds_read_b128 v[208:211], v154 offset:38912
	ds_read_b128 v[212:215], v229 offset:38912
	global_load_lds_dwordx4 v136, s[26:27]
	s_mov_b32 m0, s42
	s_nop 0
	global_load_lds_dwordx4 v132, s[26:27]
	s_waitcnt vmcnt(8)
	s_waitcnt lgkmcnt(0)
	s_barrier
	s_setprio 1
	s_waitcnt lgkmcnt(0)
	v_mfma_f32_16x16x32_bf16 v[126:129], v[146:149], v[184:187], v[126:129]
	v_mfma_f32_16x16x32_bf16 v[122:125], v[160:163], v[184:187], v[122:125]
	v_mfma_f32_16x16x32_bf16 v[110:113], v[146:149], v[192:195], v[110:113]
	v_mfma_f32_16x16x32_bf16 v[106:109], v[160:163], v[192:195], v[106:109]
	v_mfma_f32_16x16x32_bf16 v[94:97], v[146:149], v[200:203], v[94:97]
	v_mfma_f32_16x16x32_bf16 v[90:93], v[160:163], v[200:203], v[90:93]
	v_mfma_f32_16x16x32_bf16 v[78:81], v[146:149], v[208:211], v[78:81]
	v_mfma_f32_16x16x32_bf16 v[74:77], v[160:163], v[208:211], v[74:77]
	v_mfma_f32_16x16x32_bf16 v[126:129], v[156:159], v[188:191], v[126:129]
	v_mfma_f32_16x16x32_bf16 v[122:125], v[164:167], v[188:191], v[122:125]
	v_mfma_f32_16x16x32_bf16 v[110:113], v[156:159], v[196:199], v[110:113]
	v_mfma_f32_16x16x32_bf16 v[106:109], v[164:167], v[196:199], v[106:109]
	v_mfma_f32_16x16x32_bf16 v[94:97], v[156:159], v[204:207], v[94:97]
	v_mfma_f32_16x16x32_bf16 v[90:93], v[164:167], v[204:207], v[90:93]
	v_mfma_f32_16x16x32_bf16 v[78:81], v[156:159], v[212:215], v[78:81]
	v_mfma_f32_16x16x32_bf16 v[74:77], v[164:167], v[212:215], v[74:77]
	s_setprio 0
	s_setprio 1
	v_mfma_f32_16x16x32_bf16 v[118:121], v[168:171], v[184:187], v[118:121]
	v_mfma_f32_16x16x32_bf16 v[114:117], v[176:179], v[184:187], v[114:117]
	v_mfma_f32_16x16x32_bf16 v[102:105], v[168:171], v[192:195], v[102:105]
	v_mfma_f32_16x16x32_bf16 v[98:101], v[176:179], v[192:195], v[98:101]
	v_mfma_f32_16x16x32_bf16 v[86:89], v[168:171], v[200:203], v[86:89]
	v_mfma_f32_16x16x32_bf16 v[82:85], v[176:179], v[200:203], v[82:85]
	v_mfma_f32_16x16x32_bf16 v[70:73], v[168:171], v[208:211], v[70:73]
	v_mfma_f32_16x16x32_bf16 v[66:69], v[176:179], v[208:211], v[66:69]
	v_mfma_f32_16x16x32_bf16 v[118:121], v[172:175], v[188:191], v[118:121]
	v_mfma_f32_16x16x32_bf16 v[114:117], v[180:183], v[188:191], v[114:117]
	v_mfma_f32_16x16x32_bf16 v[102:105], v[172:175], v[196:199], v[102:105]
	v_mfma_f32_16x16x32_bf16 v[98:101], v[180:183], v[196:199], v[98:101]
	v_mfma_f32_16x16x32_bf16 v[86:89], v[172:175], v[204:207], v[86:89]
	v_mfma_f32_16x16x32_bf16 v[82:85], v[180:183], v[204:207], v[82:85]
	v_mfma_f32_16x16x32_bf16 v[70:73], v[172:175], v[212:215], v[70:73]
	v_mfma_f32_16x16x32_bf16 v[66:69], v[180:183], v[212:215], v[66:69]
	s_setprio 0
	s_barrier
	s_add_i32 s26, s70, s33
	v_lshl_add_u64 v[216:217], v[216:217], 0, s[8:9]
	s_mov_b32 m0, s26
	ds_read_b128 v[184:187], v154 offset:49152
	ds_read_b128 v[188:191], v229 offset:49152
	ds_read_b128 v[192:195], v154 offset:51200
	ds_read_b128 v[196:199], v229 offset:51200
	ds_read_b128 v[200:203], v154 offset:53248
	ds_read_b128 v[204:207], v229 offset:53248
	ds_read_b128 v[208:211], v154 offset:55296
	ds_read_b128 v[212:215], v229 offset:55296
	global_load_lds_dwordx4 v[216:217], off
	s_add_i32 m0, s26, 0x2000
	s_add_u32 s24, s24, 0x80080
	v_lshl_add_u64 v[216:217], v[218:219], 0, s[8:9]
	s_addc_u32 s25, s25, 0
	s_add_i32 s26, s71, s33
	global_load_lds_dwordx4 v[216:217], off
	s_mov_b32 m0, s26
	s_nop 0
	global_load_lds_dwordx4 v134, s[24:25]
	s_add_i32 m0, s26, 0x2000
	s_nop 0
	global_load_lds_dwordx4 v130, s[24:25]
	v_lshl_add_u64 v[216:217], v[220:221], 0, s[8:9]
	s_mov_b32 m0, s44
	s_nop 0
	global_load_lds_dwordx4 v[216:217], off
	v_lshl_add_u64 v[216:217], v[222:223], 0, s[8:9]
	s_mov_b32 m0, s45
	s_nop 0
	global_load_lds_dwordx4 v[216:217], off
	s_waitcnt vmcnt(8)
	s_waitcnt lgkmcnt(0)
	s_barrier
	s_setprio 1
	s_waitcnt lgkmcnt(0)
	v_mfma_f32_16x16x32_bf16 v[62:65], v[146:149], v[184:187], v[62:65]
	v_mfma_f32_16x16x32_bf16 v[58:61], v[160:163], v[184:187], v[58:61]
	v_mfma_f32_16x16x32_bf16 v[46:49], v[146:149], v[192:195], v[46:49]
	v_mfma_f32_16x16x32_bf16 v[42:45], v[160:163], v[192:195], v[42:45]
	v_mfma_f32_16x16x32_bf16 v[30:33], v[146:149], v[200:203], v[30:33]
	v_mfma_f32_16x16x32_bf16 v[26:29], v[160:163], v[200:203], v[26:29]
	v_mfma_f32_16x16x32_bf16 v[14:17], v[146:149], v[208:211], v[14:17]
	v_mfma_f32_16x16x32_bf16 v[10:13], v[160:163], v[208:211], v[10:13]
	v_mfma_f32_16x16x32_bf16 v[62:65], v[156:159], v[188:191], v[62:65]
	v_mfma_f32_16x16x32_bf16 v[58:61], v[164:167], v[188:191], v[58:61]
	v_mfma_f32_16x16x32_bf16 v[46:49], v[156:159], v[196:199], v[46:49]
	v_mfma_f32_16x16x32_bf16 v[42:45], v[164:167], v[196:199], v[42:45]
	v_mfma_f32_16x16x32_bf16 v[30:33], v[156:159], v[204:207], v[30:33]
	v_mfma_f32_16x16x32_bf16 v[26:29], v[164:167], v[204:207], v[26:29]
	v_mfma_f32_16x16x32_bf16 v[14:17], v[156:159], v[212:215], v[14:17]
	v_mfma_f32_16x16x32_bf16 v[10:13], v[164:167], v[212:215], v[10:13]
	s_setprio 0
	s_setprio 1
	v_mfma_f32_16x16x32_bf16 v[54:57], v[168:171], v[184:187], v[54:57]
	v_mfma_f32_16x16x32_bf16 v[50:53], v[176:179], v[184:187], v[50:53]
	v_mfma_f32_16x16x32_bf16 v[38:41], v[168:171], v[192:195], v[38:41]
	v_mfma_f32_16x16x32_bf16 v[34:37], v[176:179], v[192:195], v[34:37]
	v_mfma_f32_16x16x32_bf16 v[22:25], v[168:171], v[200:203], v[22:25]
	v_mfma_f32_16x16x32_bf16 v[18:21], v[176:179], v[200:203], v[18:21]
	v_mfma_f32_16x16x32_bf16 v[6:9], v[168:171], v[208:211], v[6:9]
	v_mfma_f32_16x16x32_bf16 v[2:5], v[176:179], v[208:211], v[2:5]
	v_mfma_f32_16x16x32_bf16 v[54:57], v[172:175], v[188:191], v[54:57]
	v_mfma_f32_16x16x32_bf16 v[50:53], v[180:183], v[188:191], v[50:53]
	v_mfma_f32_16x16x32_bf16 v[38:41], v[172:175], v[196:199], v[38:41]
	v_mfma_f32_16x16x32_bf16 v[34:37], v[180:183], v[196:199], v[34:37]
	v_mfma_f32_16x16x32_bf16 v[22:25], v[172:175], v[204:207], v[22:25]
	v_mfma_f32_16x16x32_bf16 v[18:21], v[180:183], v[204:207], v[18:21]
	v_mfma_f32_16x16x32_bf16 v[6:9], v[172:175], v[212:215], v[6:9]
	v_mfma_f32_16x16x32_bf16 v[2:5], v[180:183], v[212:215], v[2:5]
	s_setprio 0
	s_barrier
	s_add_i32 s69, s69, 2
	s_add_u32 s22, s22, 0x100
	s_addc_u32 s23, s23, 0
	s_add_u32 s67, s67, 0x100
	s_addc_u32 s68, s68, 0
	s_cmp_gt_u32 s69, 29
	s_cbranch_scc0 .LBB0_574
	s_nop 0
	s_nop 0
	s_nop 0
	s_nop 0
	s_nop 0
	s_nop 0
	s_nop 0
	s_nop 0
	s_nop 0
	s_nop 0
	s_nop 0
	s_nop 0
	s_nop 0
	s_nop 0
	s_and_b64 vcc, exec, s[10:11]
	s_cbranch_vccz .LBB0_577
	s_barrier
